# loop-edge: the six loop-control SALU instructions of every 8-phase K-loop moved from after the trip's closing s_barrier (head of the next load segment) to before it, in the shadow of the last MFMA; al
# baseline (speedup 1.0000x reference)
.Lpeel1f_sub3:
	s_add_i32 s75, 0, 0x18000
	s_add_i32 s76, 0, 0x1c000
	v_add_u32_e32 v12, s75, v182
	v_add_u32_e32 v28, s76, v182
	ds_read_b128 v[0:3], v12
	ds_read_b128 v[4:7], v12 offset:1024
	ds_read_b128 v[8:11], v12 offset:2048
	ds_read_b128 v[12:15], v12 offset:3072
	ds_read_b128 v[16:19], v28
	ds_read_b128 v[20:23], v28 offset:1024
	ds_read_b128 v[24:27], v28 offset:2048
	ds_read_b128 v[28:31], v28 offset:3072
	s_add_u32 s10, s10, 0x40000
	s_addc_u32 s11, s11, 0
	s_mov_b32 m0, s85
	v_lshl_add_u64 v[220:221], s[10:11], 0, v[160:161]
	ds_read_b128 v[188:191], v185 offset:32768
	ds_read_b128 v[192:195], v185 offset:33792
	ds_read_b128 v[196:199], v185 offset:34816
	ds_read_b128 v[200:203], v185 offset:35840
	ds_read_b128 v[204:207], v185 offset:36864
	ds_read_b128 v[208:211], v185 offset:37888
	ds_read_b128 v[212:215], v185 offset:38912
	ds_read_b128 v[216:219], v185 offset:39936
	global_load_lds_dwordx4 v[220:221], off
	v_lshl_add_u64 v[220:221], s[10:11], 0, v[164:165]
	s_mov_b32 m0, s86
	s_nop 0
	global_load_lds_dwordx4 v[220:221], off
	s_waitcnt vmcnt(8)
	s_waitcnt lgkmcnt(0)
	s_barrier
	s_setprio 1
	s_waitcnt lgkmcnt(0)
	v_mfma_f32_16x16x128_f8f6f4 v[156:159], v[0:7], v[188:195], v[156:159]
	v_mfma_f32_16x16x128_f8f6f4 v[152:155], v[8:15], v[188:195], v[152:155]
	v_mfma_f32_16x16x128_f8f6f4 v[140:143], v[0:7], v[196:203], v[140:143]
	v_mfma_f32_16x16x128_f8f6f4 v[136:139], v[8:15], v[196:203], v[136:139]
	v_mfma_f32_16x16x128_f8f6f4 v[124:127], v[0:7], v[204:211], v[124:127]
	v_mfma_f32_16x16x128_f8f6f4 v[120:123], v[8:15], v[204:211], v[120:123]
	v_mfma_f32_16x16x128_f8f6f4 v[108:111], v[0:7], v[212:219], v[108:111]
	v_mfma_f32_16x16x128_f8f6f4 v[104:107], v[8:15], v[212:219], v[104:107]
	s_setprio 0
	s_setprio 1
	v_mfma_f32_16x16x128_f8f6f4 v[148:151], v[16:23], v[188:195], v[148:151]
	v_mfma_f32_16x16x128_f8f6f4 v[144:147], v[24:31], v[188:195], v[144:147]
	v_mfma_f32_16x16x128_f8f6f4 v[132:135], v[16:23], v[196:203], v[132:135]
	v_mfma_f32_16x16x128_f8f6f4 v[128:131], v[24:31], v[196:203], v[128:131]
	v_mfma_f32_16x16x128_f8f6f4 v[116:119], v[16:23], v[204:211], v[116:119]
	v_mfma_f32_16x16x128_f8f6f4 v[112:115], v[24:31], v[204:211], v[112:115]
	v_mfma_f32_16x16x128_f8f6f4 v[100:103], v[16:23], v[212:219], v[100:103]
	v_mfma_f32_16x16x128_f8f6f4 v[96:99], v[24:31], v[212:219], v[96:99]
	s_setprio 0
	s_barrier
	s_add_i32 s10, s75, s38
	v_lshl_add_u64 v[174:175], v[174:175], 0, s[42:43]
	s_mov_b32 m0, s10
	ds_read_b128 v[188:191], v185 offset:49152
	ds_read_b128 v[192:195], v185 offset:50176
	ds_read_b128 v[196:199], v185 offset:51200
	ds_read_b128 v[200:203], v185 offset:52224
	ds_read_b128 v[204:207], v185 offset:53248
	ds_read_b128 v[208:211], v185 offset:54272
	ds_read_b128 v[212:215], v185 offset:55296
	ds_read_b128 v[216:219], v185 offset:56320
	global_load_lds_dwordx4 v[174:175], off
	s_add_i32 m0, s10, 0x2000
	s_add_u32 s8, s8, 0x40080
	v_lshl_add_u64 v[174:175], v[176:177], 0, s[42:43]
	s_addc_u32 s9, s9, 0
	s_add_i32 s10, s76, s38
	global_load_lds_dwordx4 v[174:175], off
	v_lshl_add_u64 v[174:175], s[8:9], 0, v[162:163]
	s_mov_b32 m0, s10
	s_nop 0
	global_load_lds_dwordx4 v[174:175], off
	v_lshl_add_u64 v[174:175], s[8:9], 0, v[166:167]
	s_add_i32 m0, s10, 0x2000
	s_nop 0
	global_load_lds_dwordx4 v[174:175], off
	v_lshl_add_u64 v[174:175], v[178:179], 0, s[42:43]
	s_mov_b32 m0, s87
	s_nop 0
	global_load_lds_dwordx4 v[174:175], off
	v_lshl_add_u64 v[174:175], v[180:181], 0, s[42:43]
	s_mov_b32 m0, s88
	s_nop 0
	global_load_lds_dwordx4 v[174:175], off
	s_waitcnt vmcnt(8)
	s_waitcnt lgkmcnt(0)
	s_barrier
	s_setprio 1
	s_waitcnt lgkmcnt(0)
	v_mfma_f32_16x16x128_f8f6f4 v[92:95], v[0:7], v[188:195], v[92:95]
	v_mfma_f32_16x16x128_f8f6f4 v[88:91], v[8:15], v[188:195], v[88:91]
	v_mfma_f32_16x16x128_f8f6f4 v[76:79], v[0:7], v[196:203], v[76:79]
	v_mfma_f32_16x16x128_f8f6f4 v[72:75], v[8:15], v[196:203], v[72:75]
	v_mfma_f32_16x16x128_f8f6f4 v[60:63], v[0:7], v[204:211], v[60:63]
	v_mfma_f32_16x16x128_f8f6f4 v[56:59], v[8:15], v[204:211], v[56:59]
	v_mfma_f32_16x16x128_f8f6f4 v[44:47], v[0:7], v[212:219], v[44:47]
	v_mfma_f32_16x16x128_f8f6f4 v[40:43], v[8:15], v[212:219], v[40:43]
	s_setprio 0
	s_setprio 1
	v_mfma_f32_16x16x128_f8f6f4 v[84:87], v[16:23], v[188:195], v[84:87]
	v_mfma_f32_16x16x128_f8f6f4 v[80:83], v[24:31], v[188:195], v[80:83]
	v_mfma_f32_16x16x128_f8f6f4 v[68:71], v[16:23], v[196:203], v[68:71]
	v_mfma_f32_16x16x128_f8f6f4 v[64:67], v[24:31], v[196:203], v[64:67]
	v_mfma_f32_16x16x128_f8f6f4 v[52:55], v[16:23], v[204:211], v[52:55]
	v_mfma_f32_16x16x128_f8f6f4 v[48:51], v[24:31], v[204:211], v[48:51]
	v_mfma_f32_16x16x128_f8f6f4 v[36:39], v[16:23], v[212:219], v[36:39]
	v_mfma_f32_16x16x128_f8f6f4 v[32:35], v[24:31], v[212:219], v[32:35]
	s_setprio 0
	s_add_i32 s74, s74, 2
	s_add_u32 s6, s6, 0x100
	s_addc_u32 s7, s7, 0
	s_add_u32 s37, s37, 0x100
	s_addc_u32 s67, s67, 0
	s_cmp_gt_u32 s74, 13
	s_barrier
	s_cbranch_scc0 .LBB0_358
	s_and_b64 vcc, exec, s[44:45]
	s_cbranch_vccz .LBB0_361
	s_barrier

.LBB0_510:
	ds_read_b128 v[24:27], v173
	ds_read_b128 v[28:31], v173 offset:1024
	ds_read_b128 v[32:35], v173 offset:2048
	ds_read_b128 v[36:39], v173 offset:3072
	ds_read_b128 v[162:165], v174
	ds_read_b128 v[166:169], v174 offset:1024
	ds_read_b128 v[178:181], v174 offset:2048
	ds_read_b128 v[182:185], v174 offset:3072
	s_add_u32 s8, s6, 0xfff80080
	s_addc_u32 s9, s7, -1
	s_cmp_eq_u32 s65, 28
	s_cselect_b32 s11, s67, s9
	s_cselect_b32 s10, s66, s8
	s_cselect_b32 s9, s69, s63
	s_cselect_b32 s8, s68, s5
	v_lshl_add_u64 v[170:171], s[6:7], 0, v[154:155]
	s_add_i32 m0, s51, 0xc000
	ds_read_b128 v[186:189], v175
	ds_read_b128 v[190:193], v175 offset:1024
	ds_read_b128 v[194:197], v175 offset:2048
	ds_read_b128 v[198:201], v175 offset:3072
	ds_read_b128 v[202:205], v175 offset:4096
	ds_read_b128 v[206:209], v175 offset:5120
	ds_read_b128 v[210:213], v175 offset:6144
	ds_read_b128 v[214:217], v175 offset:7168
	global_load_lds_dwordx4 v[170:171], off
	v_lshl_add_u64 v[170:171], s[6:7], 0, v[156:157]
	s_add_i32 m0, s51, 0xe000
	s_nop 0
	global_load_lds_dwordx4 v[170:171], off
	s_waitcnt vmcnt(8)
	s_waitcnt lgkmcnt(0)
	s_barrier
	s_setprio 1
	s_waitcnt lgkmcnt(0)
	v_mfma_f32_16x16x32_bf16 v[140:143], v[24:27], v[186:189], v[140:143]
	v_mfma_f32_16x16x32_bf16 v[136:139], v[32:35], v[186:189], v[136:139]
	v_mfma_f32_16x16x32_bf16 v[124:127], v[24:27], v[194:197], v[124:127]
	v_mfma_f32_16x16x32_bf16 v[120:123], v[32:35], v[194:197], v[120:123]
	v_mfma_f32_16x16x32_bf16 v[108:111], v[24:27], v[202:205], v[108:111]
	v_mfma_f32_16x16x32_bf16 v[104:107], v[32:35], v[202:205], v[104:107]
	v_mfma_f32_16x16x32_bf16 v[92:95], v[24:27], v[210:213], v[92:95]
	v_mfma_f32_16x16x32_bf16 v[88:91], v[32:35], v[210:213], v[88:91]
	v_mfma_f32_16x16x32_bf16 v[140:143], v[28:31], v[190:193], v[140:143]
	v_mfma_f32_16x16x32_bf16 v[136:139], v[36:39], v[190:193], v[136:139]
	v_mfma_f32_16x16x32_bf16 v[124:127], v[28:31], v[198:201], v[124:127]
	v_mfma_f32_16x16x32_bf16 v[120:123], v[36:39], v[198:201], v[120:123]
	v_mfma_f32_16x16x32_bf16 v[108:111], v[28:31], v[206:209], v[108:111]
	v_mfma_f32_16x16x32_bf16 v[104:107], v[36:39], v[206:209], v[104:107]
	v_mfma_f32_16x16x32_bf16 v[92:95], v[28:31], v[214:217], v[92:95]
	v_mfma_f32_16x16x32_bf16 v[88:91], v[36:39], v[214:217], v[88:91]
	s_setprio 0
	s_setprio 1
	v_mfma_f32_16x16x32_bf16 v[132:135], v[162:165], v[186:189], v[132:135]
	v_mfma_f32_16x16x32_bf16 v[128:131], v[178:181], v[186:189], v[128:131]
	v_mfma_f32_16x16x32_bf16 v[116:119], v[162:165], v[194:197], v[116:119]
	v_mfma_f32_16x16x32_bf16 v[112:115], v[178:181], v[194:197], v[112:115]
	v_mfma_f32_16x16x32_bf16 v[100:103], v[162:165], v[202:205], v[100:103]
	v_mfma_f32_16x16x32_bf16 v[96:99], v[178:181], v[202:205], v[96:99]
	v_mfma_f32_16x16x32_bf16 v[84:87], v[162:165], v[210:213], v[84:87]
	v_mfma_f32_16x16x32_bf16 v[80:83], v[178:181], v[210:213], v[80:83]
	v_mfma_f32_16x16x32_bf16 v[132:135], v[166:169], v[190:193], v[132:135]
	v_mfma_f32_16x16x32_bf16 v[128:131], v[182:185], v[190:193], v[128:131]
	v_mfma_f32_16x16x32_bf16 v[116:119], v[166:169], v[198:201], v[116:119]
	v_mfma_f32_16x16x32_bf16 v[112:115], v[182:185], v[198:201], v[112:115]
	v_mfma_f32_16x16x32_bf16 v[100:103], v[166:169], v[206:209], v[100:103]
	v_mfma_f32_16x16x32_bf16 v[96:99], v[182:185], v[206:209], v[96:99]
	v_mfma_f32_16x16x32_bf16 v[84:87], v[166:169], v[214:217], v[84:87]
	v_mfma_f32_16x16x32_bf16 v[80:83], v[182:185], v[214:217], v[80:83]
	s_setprio 0
	s_barrier
	s_add_i32 s70, s79, s38
	v_lshl_add_u64 v[170:171], s[8:9], 0, v[146:147]
	s_mov_b32 m0, s70
	ds_read_b128 v[186:189], v175 offset:16384
	ds_read_b128 v[190:193], v175 offset:17408
	ds_read_b128 v[194:197], v175 offset:18432
	ds_read_b128 v[198:201], v175 offset:19456
	ds_read_b128 v[202:205], v175 offset:20480
	ds_read_b128 v[206:209], v175 offset:21504
	ds_read_b128 v[210:213], v175 offset:22528
	ds_read_b128 v[214:217], v175 offset:23552
	global_load_lds_dwordx4 v[170:171], off
	s_add_i32 m0, s70, 0x2000
	s_add_u32 s70, s8, 0x80000
	v_lshl_add_u64 v[218:219], s[8:9], 0, v[150:151]
	s_addc_u32 s71, s9, 0
	s_add_i32 s72, s80, s38
	global_load_lds_dwordx4 v[218:219], off
	v_lshl_add_u64 v[220:221], s[70:71], 0, v[146:147]
	s_mov_b32 m0, s72
	v_lshl_add_u64 v[222:223], s[10:11], 0, v[148:149]
	global_load_lds_dwordx4 v[220:221], off
	v_lshl_add_u64 v[220:221], s[70:71], 0, v[150:151]
	s_add_i32 m0, s72, 0x2000
	s_nop 0
	global_load_lds_dwordx4 v[220:221], off
	v_lshl_add_u64 v[220:221], s[10:11], 0, v[144:145]
	s_mov_b32 m0, s51
	s_nop 0
	global_load_lds_dwordx4 v[220:221], off
	s_mov_b32 m0, s53
	s_nop 0
	global_load_lds_dwordx4 v[222:223], off
	s_waitcnt vmcnt(8)
	s_waitcnt lgkmcnt(0)
	s_barrier
	s_setprio 1
	s_waitcnt lgkmcnt(0)
	v_mfma_f32_16x16x32_bf16 v[76:79], v[24:27], v[186:189], v[76:79]
	v_mfma_f32_16x16x32_bf16 v[72:75], v[32:35], v[186:189], v[72:75]
	v_mfma_f32_16x16x32_bf16 v[60:63], v[24:27], v[194:197], v[60:63]
	v_mfma_f32_16x16x32_bf16 v[56:59], v[32:35], v[194:197], v[56:59]
	v_mfma_f32_16x16x32_bf16 v[44:47], v[24:27], v[202:205], v[44:47]
	v_mfma_f32_16x16x32_bf16 v[40:43], v[32:35], v[202:205], v[40:43]
	v_mfma_f32_16x16x32_bf16 v[12:15], v[24:27], v[210:213], v[12:15]
	v_mfma_f32_16x16x32_bf16 v[8:11], v[32:35], v[210:213], v[8:11]
	v_mfma_f32_16x16x32_bf16 v[76:79], v[28:31], v[190:193], v[76:79]
	v_mfma_f32_16x16x32_bf16 v[72:75], v[36:39], v[190:193], v[72:75]
	v_mfma_f32_16x16x32_bf16 v[60:63], v[28:31], v[198:201], v[60:63]
	v_mfma_f32_16x16x32_bf16 v[56:59], v[36:39], v[198:201], v[56:59]
	v_mfma_f32_16x16x32_bf16 v[44:47], v[28:31], v[206:209], v[44:47]
	v_mfma_f32_16x16x32_bf16 v[40:43], v[36:39], v[206:209], v[40:43]
	v_mfma_f32_16x16x32_bf16 v[12:15], v[28:31], v[214:217], v[12:15]
	v_mfma_f32_16x16x32_bf16 v[8:11], v[36:39], v[214:217], v[8:11]
	s_setprio 0
	s_setprio 1
	v_mfma_f32_16x16x32_bf16 v[20:23], v[162:165], v[202:205], v[20:23]
	v_mfma_f32_16x16x32_bf16 v[16:19], v[178:181], v[202:205], v[16:19]
	v_mfma_f32_16x16x32_bf16 v[4:7], v[162:165], v[210:213], v[4:7]
	v_mfma_f32_16x16x32_bf16 v[0:3], v[178:181], v[210:213], v[0:3]
	v_mfma_f32_16x16x32_bf16 v[24:27], v[162:165], v[186:189], v[68:71]
	v_mfma_f32_16x16x32_bf16 v[28:31], v[178:181], v[186:189], v[64:67]
	v_mfma_f32_16x16x32_bf16 v[32:35], v[162:165], v[194:197], v[52:55]
	v_mfma_f32_16x16x32_bf16 v[36:39], v[178:181], v[194:197], v[48:51]
	v_mfma_f32_16x16x32_bf16 v[20:23], v[166:169], v[206:209], v[20:23]
	v_mfma_f32_16x16x32_bf16 v[16:19], v[182:185], v[206:209], v[16:19]
	v_mfma_f32_16x16x32_bf16 v[4:7], v[166:169], v[214:217], v[4:7]
	v_mfma_f32_16x16x32_bf16 v[0:3], v[182:185], v[214:217], v[0:3]
	v_mfma_f32_16x16x32_bf16 v[24:27], v[166:169], v[190:193], v[24:27]
	v_mfma_f32_16x16x32_bf16 v[28:31], v[182:185], v[190:193], v[28:31]
	v_mfma_f32_16x16x32_bf16 v[32:35], v[166:169], v[198:201], v[32:35]
	v_mfma_f32_16x16x32_bf16 v[36:39], v[182:185], v[198:201], v[36:39]
	s_setprio 0
	s_barrier
	s_add_i32 s70, 0, 0x18000
	s_add_i32 s71, 0, 0x1c000
	v_add_u32_e32 v68, s70, v172
	v_add_u32_e32 v152, s71, v172
	ds_read_b128 v[48:51], v68
	ds_read_b128 v[52:55], v68 offset:1024
	ds_read_b128 v[64:67], v68 offset:2048
	ds_read_b128 v[68:71], v68 offset:3072
	ds_read_b128 v[162:165], v152
	ds_read_b128 v[166:169], v152 offset:1024
	ds_read_b128 v[178:181], v152 offset:2048
	ds_read_b128 v[182:185], v152 offset:3072
	s_add_u32 s10, s10, 0x80000
	s_addc_u32 s11, s11, 0
	s_mov_b32 m0, s55
	v_lshl_add_u64 v[224:225], s[10:11], 0, v[144:145]
	ds_read_b128 v[186:189], v175 offset:32768
	ds_read_b128 v[190:193], v175 offset:33792
	ds_read_b128 v[194:197], v175 offset:34816
	ds_read_b128 v[198:201], v175 offset:35840
	ds_read_b128 v[202:205], v175 offset:36864
	ds_read_b128 v[206:209], v175 offset:37888
	ds_read_b128 v[210:213], v175 offset:38912
	ds_read_b128 v[214:217], v175 offset:39936
	global_load_lds_dwordx4 v[224:225], off
	v_lshl_add_u64 v[224:225], s[10:11], 0, v[148:149]
	s_mov_b32 m0, s57
	s_nop 0
	global_load_lds_dwordx4 v[224:225], off
	s_waitcnt vmcnt(8)
	s_waitcnt lgkmcnt(0)
	s_barrier
	s_setprio 1
	s_waitcnt lgkmcnt(0)
	v_mfma_f32_16x16x32_bf16 v[140:143], v[48:51], v[186:189], v[140:143]
	v_mfma_f32_16x16x32_bf16 v[136:139], v[64:67], v[186:189], v[136:139]
	v_mfma_f32_16x16x32_bf16 v[124:127], v[48:51], v[194:197], v[124:127]
	v_mfma_f32_16x16x32_bf16 v[120:123], v[64:67], v[194:197], v[120:123]
	v_mfma_f32_16x16x32_bf16 v[108:111], v[48:51], v[202:205], v[108:111]
	v_mfma_f32_16x16x32_bf16 v[104:107], v[64:67], v[202:205], v[104:107]
	v_mfma_f32_16x16x32_bf16 v[92:95], v[48:51], v[210:213], v[92:95]
	v_mfma_f32_16x16x32_bf16 v[88:91], v[64:67], v[210:213], v[88:91]
	v_mfma_f32_16x16x32_bf16 v[140:143], v[52:55], v[190:193], v[140:143]
	v_mfma_f32_16x16x32_bf16 v[136:139], v[68:71], v[190:193], v[136:139]
	v_mfma_f32_16x16x32_bf16 v[124:127], v[52:55], v[198:201], v[124:127]
	v_mfma_f32_16x16x32_bf16 v[120:123], v[68:71], v[198:201], v[120:123]
	v_mfma_f32_16x16x32_bf16 v[108:111], v[52:55], v[206:209], v[108:111]
	v_mfma_f32_16x16x32_bf16 v[104:107], v[68:71], v[206:209], v[104:107]
	v_mfma_f32_16x16x32_bf16 v[92:95], v[52:55], v[214:217], v[92:95]
	v_mfma_f32_16x16x32_bf16 v[88:91], v[68:71], v[214:217], v[88:91]
	s_setprio 0
	s_setprio 1
	v_mfma_f32_16x16x32_bf16 v[132:135], v[162:165], v[186:189], v[132:135]
	v_mfma_f32_16x16x32_bf16 v[128:131], v[178:181], v[186:189], v[128:131]
	v_mfma_f32_16x16x32_bf16 v[116:119], v[162:165], v[194:197], v[116:119]
	v_mfma_f32_16x16x32_bf16 v[112:115], v[178:181], v[194:197], v[112:115]
	v_mfma_f32_16x16x32_bf16 v[100:103], v[162:165], v[202:205], v[100:103]
	v_mfma_f32_16x16x32_bf16 v[96:99], v[178:181], v[202:205], v[96:99]
	v_mfma_f32_16x16x32_bf16 v[84:87], v[162:165], v[210:213], v[84:87]
	v_mfma_f32_16x16x32_bf16 v[80:83], v[178:181], v[210:213], v[80:83]
	v_mfma_f32_16x16x32_bf16 v[132:135], v[166:169], v[190:193], v[132:135]
	v_mfma_f32_16x16x32_bf16 v[128:131], v[182:185], v[190:193], v[128:131]
	v_mfma_f32_16x16x32_bf16 v[116:119], v[166:169], v[198:201], v[116:119]
	v_mfma_f32_16x16x32_bf16 v[112:115], v[182:185], v[198:201], v[112:115]
	v_mfma_f32_16x16x32_bf16 v[100:103], v[166:169], v[206:209], v[100:103]
	v_mfma_f32_16x16x32_bf16 v[96:99], v[182:185], v[206:209], v[96:99]
	v_mfma_f32_16x16x32_bf16 v[84:87], v[166:169], v[214:217], v[84:87]
	v_mfma_f32_16x16x32_bf16 v[80:83], v[182:185], v[214:217], v[80:83]
	s_setprio 0
	s_barrier
	s_add_i32 s10, s70, s38
	v_lshl_add_u64 v[170:171], v[170:171], 0, s[40:41]
	s_mov_b32 m0, s10
	ds_read_b128 v[186:189], v175 offset:49152
	ds_read_b128 v[190:193], v175 offset:50176
	ds_read_b128 v[194:197], v175 offset:51200
	ds_read_b128 v[198:201], v175 offset:52224
	ds_read_b128 v[202:205], v175 offset:53248
	ds_read_b128 v[206:209], v175 offset:54272
	ds_read_b128 v[210:213], v175 offset:55296
	ds_read_b128 v[214:217], v175 offset:56320
	global_load_lds_dwordx4 v[170:171], off
	s_add_i32 m0, s10, 0x2000
	s_add_u32 s8, s8, 0x80080
	v_lshl_add_u64 v[170:171], v[218:219], 0, s[40:41]
	s_addc_u32 s9, s9, 0
	s_add_i32 s10, s71, s38
	global_load_lds_dwordx4 v[170:171], off
	v_lshl_add_u64 v[170:171], s[8:9], 0, v[146:147]
	s_mov_b32 m0, s10
	s_nop 0
	global_load_lds_dwordx4 v[170:171], off
	v_lshl_add_u64 v[170:171], s[8:9], 0, v[150:151]
	s_add_i32 m0, s10, 0x2000
	s_nop 0
	global_load_lds_dwordx4 v[170:171], off
	v_lshl_add_u64 v[170:171], v[220:221], 0, s[40:41]
	s_mov_b32 m0, s76
	s_nop 0
	global_load_lds_dwordx4 v[170:171], off
	v_lshl_add_u64 v[170:171], v[222:223], 0, s[40:41]
	s_mov_b32 m0, s77
	s_nop 0
	global_load_lds_dwordx4 v[170:171], off
	s_waitcnt vmcnt(8)
	s_waitcnt lgkmcnt(0)
	s_barrier
	s_setprio 1
	s_waitcnt lgkmcnt(0)
	v_mfma_f32_16x16x32_bf16 v[76:79], v[48:51], v[186:189], v[76:79]
	v_mfma_f32_16x16x32_bf16 v[72:75], v[64:67], v[186:189], v[72:75]
	v_mfma_f32_16x16x32_bf16 v[60:63], v[48:51], v[194:197], v[60:63]
	v_mfma_f32_16x16x32_bf16 v[56:59], v[64:67], v[194:197], v[56:59]
	v_mfma_f32_16x16x32_bf16 v[44:47], v[48:51], v[202:205], v[44:47]
	v_mfma_f32_16x16x32_bf16 v[40:43], v[64:67], v[202:205], v[40:43]
	v_mfma_f32_16x16x32_bf16 v[12:15], v[48:51], v[210:213], v[12:15]
	v_mfma_f32_16x16x32_bf16 v[8:11], v[64:67], v[210:213], v[8:11]
	v_mfma_f32_16x16x32_bf16 v[76:79], v[52:55], v[190:193], v[76:79]
	v_mfma_f32_16x16x32_bf16 v[72:75], v[68:71], v[190:193], v[72:75]
	v_mfma_f32_16x16x32_bf16 v[60:63], v[52:55], v[198:201], v[60:63]
	v_mfma_f32_16x16x32_bf16 v[56:59], v[68:71], v[198:201], v[56:59]
	v_mfma_f32_16x16x32_bf16 v[44:47], v[52:55], v[206:209], v[44:47]
	v_mfma_f32_16x16x32_bf16 v[40:43], v[68:71], v[206:209], v[40:43]
	v_mfma_f32_16x16x32_bf16 v[12:15], v[52:55], v[214:217], v[12:15]
	v_mfma_f32_16x16x32_bf16 v[8:11], v[68:71], v[214:217], v[8:11]
	s_setprio 0
	s_setprio 1
	v_mfma_f32_16x16x32_bf16 v[24:27], v[162:165], v[186:189], v[24:27]
	v_mfma_f32_16x16x32_bf16 v[68:71], v[166:169], v[190:193], v[24:27]
	v_mfma_f32_16x16x32_bf16 v[24:27], v[178:181], v[186:189], v[28:31]
	v_mfma_f32_16x16x32_bf16 v[64:67], v[182:185], v[190:193], v[24:27]
	v_mfma_f32_16x16x32_bf16 v[24:27], v[162:165], v[194:197], v[32:35]
	v_mfma_f32_16x16x32_bf16 v[52:55], v[166:169], v[198:201], v[24:27]
	v_mfma_f32_16x16x32_bf16 v[24:27], v[178:181], v[194:197], v[36:39]
	v_mfma_f32_16x16x32_bf16 v[20:23], v[162:165], v[202:205], v[20:23]
	v_mfma_f32_16x16x32_bf16 v[16:19], v[178:181], v[202:205], v[16:19]
	v_mfma_f32_16x16x32_bf16 v[4:7], v[162:165], v[210:213], v[4:7]
	v_mfma_f32_16x16x32_bf16 v[0:3], v[178:181], v[210:213], v[0:3]
	v_mfma_f32_16x16x32_bf16 v[48:51], v[182:185], v[198:201], v[24:27]
	v_mfma_f32_16x16x32_bf16 v[20:23], v[166:169], v[206:209], v[20:23]
	v_mfma_f32_16x16x32_bf16 v[16:19], v[182:185], v[206:209], v[16:19]
	v_mfma_f32_16x16x32_bf16 v[4:7], v[166:169], v[214:217], v[4:7]
	v_mfma_f32_16x16x32_bf16 v[0:3], v[182:185], v[214:217], v[0:3]
	s_setprio 0
	s_add_i32 s65, s65, 2
	s_add_u32 s6, s6, 0x100
	s_addc_u32 s7, s7, 0
	s_add_u32 s5, s5, 0x100
	s_addc_u32 s63, s63, 0
	s_cmp_gt_u32 s65, 29
	s_barrier
	s_cbranch_scc0 .LBB0_510
	s_and_b64 vcc, exec, s[42:43]
	s_cbranch_vccz .LBB0_513
	s_barrier

.LBB0_881:
	ds_read_b128 v[144:147], v151
	ds_read_b128 v[156:159], v151 offset:1024
	ds_read_b128 v[160:163], v151 offset:2048
	ds_read_b128 v[164:167], v151 offset:3072
	ds_read_b128 v[168:171], v152
	ds_read_b128 v[172:175], v152 offset:1024
	ds_read_b128 v[176:179], v152 offset:2048
	ds_read_b128 v[180:183], v152 offset:3072
	s_add_u32 s30, s34, 0xfffc0080
	s_addc_u32 s31, s35, -1
	s_cmp_eq_u32 s56, 12
	s_cselect_b32 s37, s25, s31
	s_cselect_b32 s36, s24, s30
	s_cselect_b32 s31, s27, s23
	s_cselect_b32 s30, s26, s21
	v_lshl_add_u64 v[148:149], s[34:35], 0, v[136:137]
	s_add_i32 m0, s29, 0xc000
	ds_read_b128 v[184:187], v153
	ds_read_b128 v[188:191], v153 offset:1024
	ds_read_b128 v[192:195], v153 offset:2048
	ds_read_b128 v[196:199], v153 offset:3072
	ds_read_b128 v[200:203], v153 offset:4096
	ds_read_b128 v[204:207], v153 offset:5120
	ds_read_b128 v[208:211], v153 offset:6144
	ds_read_b128 v[212:215], v153 offset:7168
	global_load_lds_dwordx4 v[148:149], off
	v_lshl_add_u64 v[148:149], s[34:35], 0, v[138:139]
	s_add_i32 m0, s29, 0xe000
	s_nop 0
	global_load_lds_dwordx4 v[148:149], off
	s_waitcnt vmcnt(8)
	s_waitcnt lgkmcnt(0)
	s_barrier
	s_setprio 1
	s_waitcnt lgkmcnt(0)
	v_mfma_f32_16x16x32_bf16 v[124:127], v[144:147], v[184:187], v[124:127]
	v_mfma_f32_16x16x32_bf16 v[120:123], v[160:163], v[184:187], v[120:123]
	v_mfma_f32_16x16x32_bf16 v[108:111], v[144:147], v[192:195], v[108:111]
	v_mfma_f32_16x16x32_bf16 v[104:107], v[160:163], v[192:195], v[104:107]
	v_mfma_f32_16x16x32_bf16 v[92:95], v[144:147], v[200:203], v[92:95]
	v_mfma_f32_16x16x32_bf16 v[88:91], v[160:163], v[200:203], v[88:91]
	v_mfma_f32_16x16x32_bf16 v[76:79], v[144:147], v[208:211], v[76:79]
	v_mfma_f32_16x16x32_bf16 v[72:75], v[160:163], v[208:211], v[72:75]
	v_mfma_f32_16x16x32_bf16 v[124:127], v[156:159], v[188:191], v[124:127]
	v_mfma_f32_16x16x32_bf16 v[120:123], v[164:167], v[188:191], v[120:123]
	v_mfma_f32_16x16x32_bf16 v[108:111], v[156:159], v[196:199], v[108:111]
	v_mfma_f32_16x16x32_bf16 v[104:107], v[164:167], v[196:199], v[104:107]
	v_mfma_f32_16x16x32_bf16 v[92:95], v[156:159], v[204:207], v[92:95]
	v_mfma_f32_16x16x32_bf16 v[88:91], v[164:167], v[204:207], v[88:91]
	v_mfma_f32_16x16x32_bf16 v[76:79], v[156:159], v[212:215], v[76:79]
	v_mfma_f32_16x16x32_bf16 v[72:75], v[164:167], v[212:215], v[72:75]
	s_setprio 0
	s_setprio 1
	v_mfma_f32_16x16x32_bf16 v[116:119], v[168:171], v[184:187], v[116:119]
	v_mfma_f32_16x16x32_bf16 v[112:115], v[176:179], v[184:187], v[112:115]
	v_mfma_f32_16x16x32_bf16 v[100:103], v[168:171], v[192:195], v[100:103]
	v_mfma_f32_16x16x32_bf16 v[96:99], v[176:179], v[192:195], v[96:99]
	v_mfma_f32_16x16x32_bf16 v[84:87], v[168:171], v[200:203], v[84:87]
	v_mfma_f32_16x16x32_bf16 v[80:83], v[176:179], v[200:203], v[80:83]
	v_mfma_f32_16x16x32_bf16 v[68:71], v[168:171], v[208:211], v[68:71]
	v_mfma_f32_16x16x32_bf16 v[64:67], v[176:179], v[208:211], v[64:67]
	v_mfma_f32_16x16x32_bf16 v[116:119], v[172:175], v[188:191], v[116:119]
	v_mfma_f32_16x16x32_bf16 v[112:115], v[180:183], v[188:191], v[112:115]
	v_mfma_f32_16x16x32_bf16 v[100:103], v[172:175], v[196:199], v[100:103]
	v_mfma_f32_16x16x32_bf16 v[96:99], v[180:183], v[196:199], v[96:99]
	v_mfma_f32_16x16x32_bf16 v[84:87], v[172:175], v[204:207], v[84:87]
	v_mfma_f32_16x16x32_bf16 v[80:83], v[180:183], v[204:207], v[80:83]
	v_mfma_f32_16x16x32_bf16 v[68:71], v[172:175], v[212:215], v[68:71]
	v_mfma_f32_16x16x32_bf16 v[64:67], v[180:183], v[212:215], v[64:67]
	s_setprio 0
	s_barrier
	s_add_i32 s57, s51, s38
	v_lshl_add_u64 v[148:149], s[30:31], 0, v[130:131]
	s_mov_b32 m0, s57
	ds_read_b128 v[184:187], v153 offset:16384
	ds_read_b128 v[188:191], v153 offset:17408
	ds_read_b128 v[192:195], v153 offset:18432
	ds_read_b128 v[196:199], v153 offset:19456
	ds_read_b128 v[200:203], v153 offset:20480
	ds_read_b128 v[204:207], v153 offset:21504
	ds_read_b128 v[208:211], v153 offset:22528
	ds_read_b128 v[212:215], v153 offset:23552
	global_load_lds_dwordx4 v[148:149], off
	s_add_i32 m0, s57, 0x2000
	s_add_u32 s58, s30, 0x40000
	v_lshl_add_u64 v[216:217], s[30:31], 0, v[134:135]
	s_addc_u32 s59, s31, 0
	s_add_i32 s57, s52, s38
	global_load_lds_dwordx4 v[216:217], off
	v_lshl_add_u64 v[218:219], s[58:59], 0, v[130:131]
	s_mov_b32 m0, s57
	v_lshl_add_u64 v[220:221], s[36:37], 0, v[132:133]
	global_load_lds_dwordx4 v[218:219], off
	v_lshl_add_u64 v[218:219], s[58:59], 0, v[134:135]
	s_add_i32 m0, s57, 0x2000
	s_nop 0
	global_load_lds_dwordx4 v[218:219], off
	v_lshl_add_u64 v[218:219], s[36:37], 0, v[128:129]
	s_mov_b32 m0, s29
	s_nop 0
	global_load_lds_dwordx4 v[218:219], off
	s_mov_b32 m0, s44
	s_nop 0
	global_load_lds_dwordx4 v[220:221], off
	s_waitcnt vmcnt(8)
	s_waitcnt lgkmcnt(0)
	s_barrier
	s_setprio 1
	s_waitcnt lgkmcnt(0)
	v_mfma_f32_16x16x32_bf16 v[60:63], v[144:147], v[184:187], v[60:63]
	v_mfma_f32_16x16x32_bf16 v[56:59], v[160:163], v[184:187], v[56:59]
	v_mfma_f32_16x16x32_bf16 v[44:47], v[144:147], v[192:195], v[44:47]
	v_mfma_f32_16x16x32_bf16 v[40:43], v[160:163], v[192:195], v[40:43]
	v_mfma_f32_16x16x32_bf16 v[28:31], v[144:147], v[200:203], v[28:31]
	v_mfma_f32_16x16x32_bf16 v[24:27], v[160:163], v[200:203], v[24:27]
	v_mfma_f32_16x16x32_bf16 v[12:15], v[144:147], v[208:211], v[12:15]
	v_mfma_f32_16x16x32_bf16 v[8:11], v[160:163], v[208:211], v[8:11]
	v_mfma_f32_16x16x32_bf16 v[60:63], v[156:159], v[188:191], v[60:63]
	v_mfma_f32_16x16x32_bf16 v[56:59], v[164:167], v[188:191], v[56:59]
	v_mfma_f32_16x16x32_bf16 v[44:47], v[156:159], v[196:199], v[44:47]
	v_mfma_f32_16x16x32_bf16 v[40:43], v[164:167], v[196:199], v[40:43]
	v_mfma_f32_16x16x32_bf16 v[28:31], v[156:159], v[204:207], v[28:31]
	v_mfma_f32_16x16x32_bf16 v[24:27], v[164:167], v[204:207], v[24:27]
	v_mfma_f32_16x16x32_bf16 v[12:15], v[156:159], v[212:215], v[12:15]
	v_mfma_f32_16x16x32_bf16 v[8:11], v[164:167], v[212:215], v[8:11]
	s_setprio 0
	s_setprio 1
	v_mfma_f32_16x16x32_bf16 v[52:55], v[168:171], v[184:187], v[52:55]
	v_mfma_f32_16x16x32_bf16 v[48:51], v[176:179], v[184:187], v[48:51]
	v_mfma_f32_16x16x32_bf16 v[36:39], v[168:171], v[192:195], v[36:39]
	v_mfma_f32_16x16x32_bf16 v[32:35], v[176:179], v[192:195], v[32:35]
	v_mfma_f32_16x16x32_bf16 v[20:23], v[168:171], v[200:203], v[20:23]
	v_mfma_f32_16x16x32_bf16 v[16:19], v[176:179], v[200:203], v[16:19]
	v_mfma_f32_16x16x32_bf16 v[4:7], v[168:171], v[208:211], v[4:7]
	v_mfma_f32_16x16x32_bf16 v[0:3], v[176:179], v[208:211], v[0:3]
	v_mfma_f32_16x16x32_bf16 v[52:55], v[172:175], v[188:191], v[52:55]
	v_mfma_f32_16x16x32_bf16 v[48:51], v[180:183], v[188:191], v[48:51]
	v_mfma_f32_16x16x32_bf16 v[36:39], v[172:175], v[196:199], v[36:39]
	v_mfma_f32_16x16x32_bf16 v[32:35], v[180:183], v[196:199], v[32:35]
	v_mfma_f32_16x16x32_bf16 v[20:23], v[172:175], v[204:207], v[20:23]
	v_mfma_f32_16x16x32_bf16 v[16:19], v[180:183], v[204:207], v[16:19]
	v_mfma_f32_16x16x32_bf16 v[4:7], v[172:175], v[212:215], v[4:7]
	v_mfma_f32_16x16x32_bf16 v[0:3], v[180:183], v[212:215], v[0:3]
	s_setprio 0
	s_barrier
	s_add_i32 s57, 0, 0x18000
	v_add_u32_e32 v155, s57, v150
	s_add_i32 s58, 0, 0x1c000
	ds_read_b128 v[144:147], v155
	ds_read_b128 v[156:159], v155 offset:1024
	ds_read_b128 v[160:163], v155 offset:2048
	ds_read_b128 v[164:167], v155 offset:3072
	v_add_u32_e32 v155, s58, v150
	ds_read_b128 v[168:171], v155
	ds_read_b128 v[172:175], v155 offset:1024
	ds_read_b128 v[176:179], v155 offset:2048
	ds_read_b128 v[180:183], v155 offset:3072
	s_add_u32 s36, s36, 0x40000
	s_addc_u32 s37, s37, 0
	s_mov_b32 m0, s45
	v_lshl_add_u64 v[222:223], s[36:37], 0, v[128:129]
	ds_read_b128 v[184:187], v153 offset:32768
	ds_read_b128 v[188:191], v153 offset:33792
	ds_read_b128 v[192:195], v153 offset:34816
	ds_read_b128 v[196:199], v153 offset:35840
	ds_read_b128 v[200:203], v153 offset:36864
	ds_read_b128 v[204:207], v153 offset:37888
	ds_read_b128 v[208:211], v153 offset:38912
	ds_read_b128 v[212:215], v153 offset:39936
	global_load_lds_dwordx4 v[222:223], off
	v_lshl_add_u64 v[222:223], s[36:37], 0, v[132:133]
	s_mov_b32 m0, s48
	s_nop 0
	global_load_lds_dwordx4 v[222:223], off
	s_waitcnt vmcnt(8)
	s_waitcnt lgkmcnt(0)
	s_barrier
	s_setprio 1
	s_waitcnt lgkmcnt(0)
	v_mfma_f32_16x16x32_bf16 v[124:127], v[144:147], v[184:187], v[124:127]
	v_mfma_f32_16x16x32_bf16 v[120:123], v[160:163], v[184:187], v[120:123]
	v_mfma_f32_16x16x32_bf16 v[108:111], v[144:147], v[192:195], v[108:111]
	v_mfma_f32_16x16x32_bf16 v[104:107], v[160:163], v[192:195], v[104:107]
	v_mfma_f32_16x16x32_bf16 v[92:95], v[144:147], v[200:203], v[92:95]
	v_mfma_f32_16x16x32_bf16 v[88:91], v[160:163], v[200:203], v[88:91]
	v_mfma_f32_16x16x32_bf16 v[76:79], v[144:147], v[208:211], v[76:79]
	v_mfma_f32_16x16x32_bf16 v[72:75], v[160:163], v[208:211], v[72:75]
	v_mfma_f32_16x16x32_bf16 v[124:127], v[156:159], v[188:191], v[124:127]
	v_mfma_f32_16x16x32_bf16 v[120:123], v[164:167], v[188:191], v[120:123]
	v_mfma_f32_16x16x32_bf16 v[108:111], v[156:159], v[196:199], v[108:111]
	v_mfma_f32_16x16x32_bf16 v[104:107], v[164:167], v[196:199], v[104:107]
	v_mfma_f32_16x16x32_bf16 v[92:95], v[156:159], v[204:207], v[92:95]
	v_mfma_f32_16x16x32_bf16 v[88:91], v[164:167], v[204:207], v[88:91]
	v_mfma_f32_16x16x32_bf16 v[76:79], v[156:159], v[212:215], v[76:79]
	v_mfma_f32_16x16x32_bf16 v[72:75], v[164:167], v[212:215], v[72:75]
	s_setprio 0
	s_setprio 1
	v_mfma_f32_16x16x32_bf16 v[116:119], v[168:171], v[184:187], v[116:119]
	v_mfma_f32_16x16x32_bf16 v[112:115], v[176:179], v[184:187], v[112:115]
	v_mfma_f32_16x16x32_bf16 v[100:103], v[168:171], v[192:195], v[100:103]
	v_mfma_f32_16x16x32_bf16 v[96:99], v[176:179], v[192:195], v[96:99]
	v_mfma_f32_16x16x32_bf16 v[84:87], v[168:171], v[200:203], v[84:87]
	v_mfma_f32_16x16x32_bf16 v[80:83], v[176:179], v[200:203], v[80:83]
	v_mfma_f32_16x16x32_bf16 v[68:71], v[168:171], v[208:211], v[68:71]
	v_mfma_f32_16x16x32_bf16 v[64:67], v[176:179], v[208:211], v[64:67]
	v_mfma_f32_16x16x32_bf16 v[116:119], v[172:175], v[188:191], v[116:119]
	v_mfma_f32_16x16x32_bf16 v[112:115], v[180:183], v[188:191], v[112:115]
	v_mfma_f32_16x16x32_bf16 v[100:103], v[172:175], v[196:199], v[100:103]
	v_mfma_f32_16x16x32_bf16 v[96:99], v[180:183], v[196:199], v[96:99]
	v_mfma_f32_16x16x32_bf16 v[84:87], v[172:175], v[204:207], v[84:87]
	v_mfma_f32_16x16x32_bf16 v[80:83], v[180:183], v[204:207], v[80:83]
	v_mfma_f32_16x16x32_bf16 v[68:71], v[172:175], v[212:215], v[68:71]
	v_mfma_f32_16x16x32_bf16 v[64:67], v[180:183], v[212:215], v[64:67]
	s_setprio 0
	s_barrier
	s_add_i32 s36, s57, s38
	v_lshl_add_u64 v[148:149], v[148:149], 0, s[12:13]
	s_mov_b32 m0, s36
	ds_read_b128 v[184:187], v153 offset:49152
	ds_read_b128 v[188:191], v153 offset:50176
	ds_read_b128 v[192:195], v153 offset:51200
	ds_read_b128 v[196:199], v153 offset:52224
	ds_read_b128 v[200:203], v153 offset:53248
	ds_read_b128 v[204:207], v153 offset:54272
	ds_read_b128 v[208:211], v153 offset:55296
	ds_read_b128 v[212:215], v153 offset:56320
	global_load_lds_dwordx4 v[148:149], off
	s_add_i32 m0, s36, 0x2000
	s_add_u32 s30, s30, 0x40080
	v_lshl_add_u64 v[148:149], v[216:217], 0, s[12:13]
	s_addc_u32 s31, s31, 0
	s_add_i32 s36, s58, s38
	global_load_lds_dwordx4 v[148:149], off
	v_lshl_add_u64 v[148:149], s[30:31], 0, v[130:131]
	s_mov_b32 m0, s36
	s_nop 0
	global_load_lds_dwordx4 v[148:149], off
	v_lshl_add_u64 v[148:149], s[30:31], 0, v[134:135]
	s_add_i32 m0, s36, 0x2000
	s_nop 0
	global_load_lds_dwordx4 v[148:149], off
	v_lshl_add_u64 v[148:149], v[218:219], 0, s[12:13]
	s_mov_b32 m0, s47
	s_nop 0
	global_load_lds_dwordx4 v[148:149], off
	v_lshl_add_u64 v[148:149], v[220:221], 0, s[12:13]
	s_mov_b32 m0, s50
	s_nop 0
	global_load_lds_dwordx4 v[148:149], off
	s_waitcnt vmcnt(8)
	s_waitcnt lgkmcnt(0)
	s_barrier
	s_setprio 1
	s_waitcnt lgkmcnt(0)
	v_mfma_f32_16x16x32_bf16 v[60:63], v[144:147], v[184:187], v[60:63]
	v_mfma_f32_16x16x32_bf16 v[56:59], v[160:163], v[184:187], v[56:59]
	v_mfma_f32_16x16x32_bf16 v[44:47], v[144:147], v[192:195], v[44:47]
	v_mfma_f32_16x16x32_bf16 v[40:43], v[160:163], v[192:195], v[40:43]
	v_mfma_f32_16x16x32_bf16 v[28:31], v[144:147], v[200:203], v[28:31]
	v_mfma_f32_16x16x32_bf16 v[24:27], v[160:163], v[200:203], v[24:27]
	v_mfma_f32_16x16x32_bf16 v[12:15], v[144:147], v[208:211], v[12:15]
	v_mfma_f32_16x16x32_bf16 v[8:11], v[160:163], v[208:211], v[8:11]
	v_mfma_f32_16x16x32_bf16 v[60:63], v[156:159], v[188:191], v[60:63]
	v_mfma_f32_16x16x32_bf16 v[56:59], v[164:167], v[188:191], v[56:59]
	v_mfma_f32_16x16x32_bf16 v[44:47], v[156:159], v[196:199], v[44:47]
	v_mfma_f32_16x16x32_bf16 v[40:43], v[164:167], v[196:199], v[40:43]
	v_mfma_f32_16x16x32_bf16 v[28:31], v[156:159], v[204:207], v[28:31]
	v_mfma_f32_16x16x32_bf16 v[24:27], v[164:167], v[204:207], v[24:27]
	v_mfma_f32_16x16x32_bf16 v[12:15], v[156:159], v[212:215], v[12:15]
	v_mfma_f32_16x16x32_bf16 v[8:11], v[164:167], v[212:215], v[8:11]
	s_setprio 0
	s_setprio 1
	v_mfma_f32_16x16x32_bf16 v[52:55], v[168:171], v[184:187], v[52:55]
	v_mfma_f32_16x16x32_bf16 v[48:51], v[176:179], v[184:187], v[48:51]
	v_mfma_f32_16x16x32_bf16 v[36:39], v[168:171], v[192:195], v[36:39]
	v_mfma_f32_16x16x32_bf16 v[32:35], v[176:179], v[192:195], v[32:35]
	v_mfma_f32_16x16x32_bf16 v[20:23], v[168:171], v[200:203], v[20:23]
	v_mfma_f32_16x16x32_bf16 v[16:19], v[176:179], v[200:203], v[16:19]
	v_mfma_f32_16x16x32_bf16 v[4:7], v[168:171], v[208:211], v[4:7]
	v_mfma_f32_16x16x32_bf16 v[0:3], v[176:179], v[208:211], v[0:3]
	v_mfma_f32_16x16x32_bf16 v[52:55], v[172:175], v[188:191], v[52:55]
	v_mfma_f32_16x16x32_bf16 v[48:51], v[180:183], v[188:191], v[48:51]
	v_mfma_f32_16x16x32_bf16 v[36:39], v[172:175], v[196:199], v[36:39]
	v_mfma_f32_16x16x32_bf16 v[32:35], v[180:183], v[196:199], v[32:35]
	v_mfma_f32_16x16x32_bf16 v[20:23], v[172:175], v[204:207], v[20:23]
	v_mfma_f32_16x16x32_bf16 v[16:19], v[180:183], v[204:207], v[16:19]
	v_mfma_f32_16x16x32_bf16 v[4:7], v[172:175], v[212:215], v[4:7]
	v_mfma_f32_16x16x32_bf16 v[0:3], v[180:183], v[212:215], v[0:3]
	s_setprio 0
	s_add_i32 s56, s56, 2
	s_add_u32 s34, s34, 0x100
	s_addc_u32 s35, s35, 0
	s_add_u32 s21, s21, 0x100
	s_addc_u32 s23, s23, 0
	s_cmp_gt_u32 s56, 13
	s_barrier
	s_cbranch_scc0 .LBB0_881
	s_and_b64 vcc, exec, s[14:15]
	s_cbranch_vccz .LBB0_884
	s_barrier

.Lpeel5_sub3:
	s_add_i32 s39, 0, 0x18000
	s_add_i32 s60, 0, 0x1c000
	v_add_u32_e32 v12, s39, v184
	v_add_u32_e32 v28, s60, v184
	ds_read_b128 v[0:3], v12
	ds_read_b128 v[4:7], v12 offset:1024
	ds_read_b128 v[8:11], v12 offset:2048
	ds_read_b128 v[12:15], v12 offset:3072
	ds_read_b128 v[16:19], v28
	ds_read_b128 v[20:23], v28 offset:1024
	ds_read_b128 v[24:27], v28 offset:2048
	ds_read_b128 v[28:31], v28 offset:3072
	s_add_u32 s36, s36, 0x40000
	s_addc_u32 s37, s37, 0
	s_mov_b32 m0, s49
	v_lshl_add_u64 v[220:221], s[36:37], 0, v[160:161]
	ds_read_b128 v[188:191], v187 offset:32768
	ds_read_b128 v[192:195], v187 offset:33792
	ds_read_b128 v[196:199], v187 offset:34816
	ds_read_b128 v[200:203], v187 offset:35840
	ds_read_b128 v[204:207], v187 offset:36864
	ds_read_b128 v[208:211], v187 offset:37888
	ds_read_b128 v[212:215], v187 offset:38912
	ds_read_b128 v[216:219], v187 offset:39936
	global_load_lds_dwordx4 v[220:221], off
	v_lshl_add_u64 v[220:221], s[36:37], 0, v[164:165]
	s_mov_b32 m0, s50
	s_nop 0
	global_load_lds_dwordx4 v[220:221], off
	s_waitcnt vmcnt(8)
	s_waitcnt lgkmcnt(0)
	s_barrier
	s_setprio 1
	s_waitcnt lgkmcnt(0)
	v_mfma_f32_16x16x128_f8f6f4 v[156:159], v[0:7], v[188:195], v[156:159]
	v_mfma_f32_16x16x128_f8f6f4 v[152:155], v[8:15], v[188:195], v[152:155]
	v_mfma_f32_16x16x128_f8f6f4 v[140:143], v[0:7], v[196:203], v[140:143]
	v_mfma_f32_16x16x128_f8f6f4 v[136:139], v[8:15], v[196:203], v[136:139]
	v_mfma_f32_16x16x128_f8f6f4 v[124:127], v[0:7], v[204:211], v[124:127]
	v_mfma_f32_16x16x128_f8f6f4 v[120:123], v[8:15], v[204:211], v[120:123]
	v_mfma_f32_16x16x128_f8f6f4 v[108:111], v[0:7], v[212:219], v[108:111]
	v_mfma_f32_16x16x128_f8f6f4 v[104:107], v[8:15], v[212:219], v[104:107]
	s_setprio 0
	s_setprio 1
	v_mfma_f32_16x16x128_f8f6f4 v[148:151], v[16:23], v[188:195], v[148:151]
	v_mfma_f32_16x16x128_f8f6f4 v[144:147], v[24:31], v[188:195], v[144:147]
	v_mfma_f32_16x16x128_f8f6f4 v[132:135], v[16:23], v[196:203], v[132:135]
	v_mfma_f32_16x16x128_f8f6f4 v[128:131], v[24:31], v[196:203], v[128:131]
	v_mfma_f32_16x16x128_f8f6f4 v[116:119], v[16:23], v[204:211], v[116:119]
	v_mfma_f32_16x16x128_f8f6f4 v[112:115], v[24:31], v[204:211], v[112:115]
	v_mfma_f32_16x16x128_f8f6f4 v[100:103], v[16:23], v[212:219], v[100:103]
	v_mfma_f32_16x16x128_f8f6f4 v[96:99], v[24:31], v[212:219], v[96:99]
	s_setprio 0
	s_barrier
	s_add_i32 s36, s39, s47
	v_lshl_add_u64 v[176:177], v[176:177], 0, s[10:11]
	s_mov_b32 m0, s36
	ds_read_b128 v[188:191], v187 offset:49152
	ds_read_b128 v[192:195], v187 offset:50176
	ds_read_b128 v[196:199], v187 offset:51200
	ds_read_b128 v[200:203], v187 offset:52224
	ds_read_b128 v[204:207], v187 offset:53248
	ds_read_b128 v[208:211], v187 offset:54272
	ds_read_b128 v[212:215], v187 offset:55296
	ds_read_b128 v[216:219], v187 offset:56320
	global_load_lds_dwordx4 v[176:177], off
	s_add_i32 m0, s36, 0x2000
	s_add_u32 s30, s30, 0x40080
	v_lshl_add_u64 v[176:177], v[178:179], 0, s[10:11]
	s_addc_u32 s31, s31, 0
	s_add_i32 s36, s60, s47
	global_load_lds_dwordx4 v[176:177], off
	v_lshl_add_u64 v[176:177], s[30:31], 0, v[162:163]
	s_mov_b32 m0, s36
	s_nop 0
	global_load_lds_dwordx4 v[176:177], off
	v_lshl_add_u64 v[176:177], s[30:31], 0, v[166:167]
	s_add_i32 m0, s36, 0x2000
	s_nop 0
	global_load_lds_dwordx4 v[176:177], off
	v_lshl_add_u64 v[176:177], v[180:181], 0, s[10:11]
	s_mov_b32 m0, s54
	s_nop 0
	global_load_lds_dwordx4 v[176:177], off
	v_lshl_add_u64 v[176:177], v[182:183], 0, s[10:11]
	s_mov_b32 m0, s55
	s_nop 0
	global_load_lds_dwordx4 v[176:177], off
	s_waitcnt vmcnt(8)
	s_waitcnt lgkmcnt(0)
	s_barrier
	s_setprio 1
	s_waitcnt lgkmcnt(0)
	v_mfma_f32_16x16x128_f8f6f4 v[92:95], v[0:7], v[188:195], v[92:95]
	v_mfma_f32_16x16x128_f8f6f4 v[88:91], v[8:15], v[188:195], v[88:91]
	v_mfma_f32_16x16x128_f8f6f4 v[76:79], v[0:7], v[196:203], v[76:79]
	v_mfma_f32_16x16x128_f8f6f4 v[72:75], v[8:15], v[196:203], v[72:75]
	v_mfma_f32_16x16x128_f8f6f4 v[60:63], v[0:7], v[204:211], v[60:63]
	v_mfma_f32_16x16x128_f8f6f4 v[56:59], v[8:15], v[204:211], v[56:59]
	v_mfma_f32_16x16x128_f8f6f4 v[44:47], v[0:7], v[212:219], v[44:47]
	v_mfma_f32_16x16x128_f8f6f4 v[40:43], v[8:15], v[212:219], v[40:43]
	s_setprio 0
	s_setprio 1
	v_mfma_f32_16x16x128_f8f6f4 v[84:87], v[16:23], v[188:195], v[84:87]
	v_mfma_f32_16x16x128_f8f6f4 v[80:83], v[24:31], v[188:195], v[80:83]
	v_mfma_f32_16x16x128_f8f6f4 v[68:71], v[16:23], v[196:203], v[68:71]
	v_mfma_f32_16x16x128_f8f6f4 v[64:67], v[24:31], v[196:203], v[64:67]
	v_mfma_f32_16x16x128_f8f6f4 v[52:55], v[16:23], v[204:211], v[52:55]
	v_mfma_f32_16x16x128_f8f6f4 v[48:51], v[24:31], v[204:211], v[48:51]
	v_mfma_f32_16x16x128_f8f6f4 v[36:39], v[16:23], v[212:219], v[36:39]
	v_mfma_f32_16x16x128_f8f6f4 v[32:35], v[24:31], v[212:219], v[32:35]
	s_setprio 0
	s_add_i32 s38, s38, 2
	s_add_u32 s42, s42, 0x100
	s_addc_u32 s43, s43, 0
	s_add_u32 s25, s25, 0x100
	s_addc_u32 s27, s27, 0
	s_cmp_gt_u32 s38, 13
	s_barrier
	s_cbranch_scc0 .LBB0_958
	s_and_b64 vcc, exec, s[12:13]
	s_cbranch_vccz .LBB0_961
	s_barrier

.Lpeel8_sub3:
	s_add_i32 s64, 0, 0x18000
	s_add_i32 s65, 0, 0x1c000
	v_add_u32_e32 v12, s64, v236
	v_add_u32_e32 v28, s65, v236
	ds_read_b128 v[0:3], v12
	ds_read_b128 v[4:7], v12 offset:1024
	ds_read_b128 v[8:11], v12 offset:2048
	ds_read_b128 v[12:15], v12 offset:3072
	ds_read_b128 v[16:19], v28
	ds_read_b128 v[20:23], v28 offset:1024
	ds_read_b128 v[24:27], v28 offset:2048
	ds_read_b128 v[28:31], v28 offset:3072
	s_mov_b32 m0, s45
	v_lshl_add_u64 v[248:249], s[36:37], 0, v[216:217]
	ds_read_b128 v[40:43], v237 offset:32768
	ds_read_b128 v[44:47], v237 offset:33792
	ds_read_b128 v[48:51], v237 offset:34816
	ds_read_b128 v[52:55], v237 offset:35840
	ds_read_b128 v[56:59], v237 offset:36864
	ds_read_b128 v[60:63], v237 offset:37888
	ds_read_b128 v[240:243], v237 offset:38912
	ds_read_b128 v[244:247], v237 offset:39936
	global_load_lds_dwordx4 v[248:249], off
	v_lshl_add_u64 v[248:249], s[36:37], 0, v[218:219]
	s_mov_b32 m0, s46
	s_nop 0
	global_load_lds_dwordx4 v[248:249], off
	s_waitcnt vmcnt(8)
	s_waitcnt lgkmcnt(0)
	s_barrier
	s_setprio 1
	s_waitcnt lgkmcnt(0)
	v_mfma_f32_16x16x128_f8f6f4 v[204:207], v[0:7], v[40:47], v[204:207]
	v_mfma_f32_16x16x128_f8f6f4 v[196:199], v[8:15], v[40:47], v[196:199]
	v_mfma_f32_16x16x128_f8f6f4 v[188:191], v[0:7], v[48:55], v[188:191]
	v_mfma_f32_16x16x128_f8f6f4 v[180:183], v[8:15], v[48:55], v[180:183]
	v_mfma_f32_16x16x128_f8f6f4 v[172:175], v[0:7], v[56:63], v[172:175]
	v_mfma_f32_16x16x128_f8f6f4 v[164:167], v[8:15], v[56:63], v[164:167]
	v_mfma_f32_16x16x128_f8f6f4 v[156:159], v[0:7], v[240:247], v[156:159]
	v_mfma_f32_16x16x128_f8f6f4 v[148:151], v[8:15], v[240:247], v[148:151]
	s_setprio 0
	s_setprio 1
	v_mfma_f32_16x16x128_f8f6f4 v[200:203], v[16:23], v[40:47], v[200:203]
	v_mfma_f32_16x16x128_f8f6f4 v[192:195], v[24:31], v[40:47], v[192:195]
	v_mfma_f32_16x16x128_f8f6f4 v[184:187], v[16:23], v[48:55], v[184:187]
	v_mfma_f32_16x16x128_f8f6f4 v[176:179], v[24:31], v[48:55], v[176:179]
	v_mfma_f32_16x16x128_f8f6f4 v[168:171], v[16:23], v[56:63], v[168:171]
	v_mfma_f32_16x16x128_f8f6f4 v[160:163], v[24:31], v[56:63], v[160:163]
	v_mfma_f32_16x16x128_f8f6f4 v[152:155], v[16:23], v[240:247], v[152:155]
	v_mfma_f32_16x16x128_f8f6f4 v[144:147], v[24:31], v[240:247], v[144:147]
	s_setprio 0
	s_barrier
	s_add_i32 s36, s64, s38
	v_lshl_add_u64 v[34:35], v[34:35], 0, s[12:13]
	s_mov_b32 m0, s36
	ds_read_b128 v[40:43], v237 offset:49152
	ds_read_b128 v[44:47], v237 offset:50176
	ds_read_b128 v[48:51], v237 offset:51200
	ds_read_b128 v[52:55], v237 offset:52224
	ds_read_b128 v[56:59], v237 offset:53248
	ds_read_b128 v[60:63], v237 offset:54272
	ds_read_b128 v[240:243], v237 offset:55296
	ds_read_b128 v[244:247], v237 offset:56320
	global_load_lds_dwordx4 v[34:35], off
	s_add_i32 m0, s36, 0x2000
	s_add_u32 s30, s30, 0x40080
	v_lshl_add_u64 v[32:33], v[32:33], 0, s[12:13]
	s_addc_u32 s31, s31, 0
	s_add_i32 s36, s65, s38
	global_load_lds_dwordx4 v[32:33], off
	v_lshl_add_u64 v[32:33], s[30:31], 0, v[208:209]
	s_mov_b32 m0, s36
	s_nop 0
	global_load_lds_dwordx4 v[32:33], off
	v_lshl_add_u64 v[32:33], s[30:31], 0, v[210:211]
	s_add_i32 m0, s36, 0x2000
	s_nop 0
	global_load_lds_dwordx4 v[32:33], off
	v_lshl_add_u64 v[32:33], v[38:39], 0, s[12:13]
	s_mov_b32 m0, s50
	s_nop 0
	global_load_lds_dwordx4 v[32:33], off
	v_lshl_add_u64 v[32:33], v[36:37], 0, s[12:13]
	s_mov_b32 m0, s51
	s_nop 0
	global_load_lds_dwordx4 v[32:33], off
	s_waitcnt vmcnt(8)
	s_waitcnt lgkmcnt(0)
	s_barrier
	s_setprio 1
	s_waitcnt lgkmcnt(0)
	v_mfma_f32_16x16x128_f8f6f4 v[140:143], v[0:7], v[40:47], v[140:143]
	v_mfma_f32_16x16x128_f8f6f4 v[132:135], v[8:15], v[40:47], v[132:135]
	v_mfma_f32_16x16x128_f8f6f4 v[124:127], v[0:7], v[48:55], v[124:127]
	v_mfma_f32_16x16x128_f8f6f4 v[116:119], v[8:15], v[48:55], v[116:119]
	v_mfma_f32_16x16x128_f8f6f4 v[108:111], v[0:7], v[56:63], v[108:111]
	v_mfma_f32_16x16x128_f8f6f4 v[100:103], v[8:15], v[56:63], v[100:103]
	v_mfma_f32_16x16x128_f8f6f4 v[92:95], v[0:7], v[240:247], v[92:95]
	v_mfma_f32_16x16x128_f8f6f4 v[84:87], v[8:15], v[240:247], v[84:87]
	s_setprio 0
	s_setprio 1
	v_mfma_f32_16x16x128_f8f6f4 v[136:139], v[16:23], v[40:47], v[136:139]
	v_mfma_f32_16x16x128_f8f6f4 v[128:131], v[24:31], v[40:47], v[128:131]
	v_mfma_f32_16x16x128_f8f6f4 v[120:123], v[16:23], v[48:55], v[120:123]
	v_mfma_f32_16x16x128_f8f6f4 v[112:115], v[24:31], v[48:55], v[112:115]
	v_mfma_f32_16x16x128_f8f6f4 v[104:107], v[16:23], v[56:63], v[104:107]
	v_mfma_f32_16x16x128_f8f6f4 v[96:99], v[24:31], v[56:63], v[96:99]
	v_mfma_f32_16x16x128_f8f6f4 v[88:91], v[16:23], v[240:247], v[88:91]
	v_mfma_f32_16x16x128_f8f6f4 v[80:83], v[24:31], v[240:247], v[80:83]
	s_setprio 0
	s_add_i32 s63, s63, 2
	s_add_u32 s34, s34, 0x100
	s_addc_u32 s35, s35, 0
	s_add_u32 s23, s23, 0x100
	s_addc_u32 s29, s29, 0
	s_cmp_gt_u32 s63, 13
	s_barrier
	s_cbranch_scc1 .LBB0_1194

.Lpeel9_sub3:
	s_add_i32 s38, 0, 0x18000
	s_add_i32 s39, 0, 0x1c000
	v_add_u32_e32 v12, s38, v186
	v_add_u32_e32 v28, s39, v186
	ds_read_b128 v[0:3], v12
	ds_read_b128 v[4:7], v12 offset:1024
	ds_read_b128 v[8:11], v12 offset:2048
	ds_read_b128 v[12:15], v12 offset:3072
	ds_read_b128 v[16:19], v28
	ds_read_b128 v[20:23], v28 offset:1024
	ds_read_b128 v[24:27], v28 offset:2048
	ds_read_b128 v[28:31], v28 offset:3072
	s_add_u32 s36, s36, 0x40000
	s_addc_u32 s37, s37, 0
	s_mov_b32 m0, s64
	v_lshl_add_u64 v[222:223], s[36:37], 0, v[162:163]
	ds_read_b128 v[190:193], v187 offset:32768
	ds_read_b128 v[194:197], v187 offset:33792
	ds_read_b128 v[198:201], v187 offset:34816
	ds_read_b128 v[202:205], v187 offset:35840
	ds_read_b128 v[206:209], v187 offset:36864
	ds_read_b128 v[210:213], v187 offset:37888
	ds_read_b128 v[214:217], v187 offset:38912
	ds_read_b128 v[218:221], v187 offset:39936
	global_load_lds_dwordx4 v[222:223], off
	v_lshl_add_u64 v[222:223], s[36:37], 0, v[166:167]
	s_mov_b32 m0, s65
	s_nop 0
	global_load_lds_dwordx4 v[222:223], off
	s_waitcnt vmcnt(8)
	s_waitcnt lgkmcnt(0)
	s_barrier
	s_setprio 1
	s_waitcnt lgkmcnt(0)
	v_mfma_f32_16x16x128_f8f6f4 v[156:159], v[0:7], v[190:197], v[156:159]
	v_mfma_f32_16x16x128_f8f6f4 v[152:155], v[8:15], v[190:197], v[152:155]
	v_mfma_f32_16x16x128_f8f6f4 v[140:143], v[0:7], v[198:205], v[140:143]
	v_mfma_f32_16x16x128_f8f6f4 v[136:139], v[8:15], v[198:205], v[136:139]
	v_mfma_f32_16x16x128_f8f6f4 v[124:127], v[0:7], v[206:213], v[124:127]
	v_mfma_f32_16x16x128_f8f6f4 v[120:123], v[8:15], v[206:213], v[120:123]
	v_mfma_f32_16x16x128_f8f6f4 v[108:111], v[0:7], v[214:221], v[108:111]
	v_mfma_f32_16x16x128_f8f6f4 v[104:107], v[8:15], v[214:221], v[104:107]
	s_setprio 0
	s_setprio 1
	v_mfma_f32_16x16x128_f8f6f4 v[148:151], v[16:23], v[190:197], v[148:151]
	v_mfma_f32_16x16x128_f8f6f4 v[144:147], v[24:31], v[190:197], v[144:147]
	v_mfma_f32_16x16x128_f8f6f4 v[132:135], v[16:23], v[198:205], v[132:135]
	v_mfma_f32_16x16x128_f8f6f4 v[128:131], v[24:31], v[198:205], v[128:131]
	v_mfma_f32_16x16x128_f8f6f4 v[116:119], v[16:23], v[206:213], v[116:119]
	v_mfma_f32_16x16x128_f8f6f4 v[112:115], v[24:31], v[206:213], v[112:115]
	v_mfma_f32_16x16x128_f8f6f4 v[100:103], v[16:23], v[214:221], v[100:103]
	v_mfma_f32_16x16x128_f8f6f4 v[96:99], v[24:31], v[214:221], v[96:99]
	s_setprio 0
	s_barrier
	s_add_i32 s36, s38, s47
	v_lshl_add_u64 v[178:179], v[178:179], 0, s[14:15]
	s_mov_b32 m0, s36
	ds_read_b128 v[190:193], v187 offset:49152
	ds_read_b128 v[194:197], v187 offset:50176
	ds_read_b128 v[198:201], v187 offset:51200
	ds_read_b128 v[202:205], v187 offset:52224
	ds_read_b128 v[206:209], v187 offset:53248
	ds_read_b128 v[210:213], v187 offset:54272
	ds_read_b128 v[214:217], v187 offset:55296
	ds_read_b128 v[218:221], v187 offset:56320
	global_load_lds_dwordx4 v[178:179], off
	s_add_i32 m0, s36, 0x2000
	s_add_u32 s30, s30, 0x40080
	v_lshl_add_u64 v[178:179], v[180:181], 0, s[14:15]
	s_addc_u32 s31, s31, 0
	s_add_i32 s36, s39, s47
	global_load_lds_dwordx4 v[178:179], off
	v_lshl_add_u64 v[178:179], s[30:31], 0, v[164:165]
	s_mov_b32 m0, s36
	s_nop 0
	global_load_lds_dwordx4 v[178:179], off
	v_lshl_add_u64 v[178:179], s[30:31], 0, v[168:169]
	s_add_i32 m0, s36, 0x2000
	s_nop 0
	global_load_lds_dwordx4 v[178:179], off
	v_lshl_add_u64 v[178:179], v[182:183], 0, s[14:15]
	s_mov_b32 m0, s66
	s_nop 0
	global_load_lds_dwordx4 v[178:179], off
	v_lshl_add_u64 v[178:179], v[184:185], 0, s[14:15]
	s_mov_b32 m0, s67
	s_nop 0
	global_load_lds_dwordx4 v[178:179], off
	s_waitcnt vmcnt(8)
	s_waitcnt lgkmcnt(0)
	s_barrier
	s_setprio 1
	s_waitcnt lgkmcnt(0)
	v_mfma_f32_16x16x128_f8f6f4 v[92:95], v[0:7], v[190:197], v[92:95]
	v_mfma_f32_16x16x128_f8f6f4 v[88:91], v[8:15], v[190:197], v[88:91]
	v_mfma_f32_16x16x128_f8f6f4 v[76:79], v[0:7], v[198:205], v[76:79]
	v_mfma_f32_16x16x128_f8f6f4 v[72:75], v[8:15], v[198:205], v[72:75]
	v_mfma_f32_16x16x128_f8f6f4 v[60:63], v[0:7], v[206:213], v[60:63]
	v_mfma_f32_16x16x128_f8f6f4 v[56:59], v[8:15], v[206:213], v[56:59]
	v_mfma_f32_16x16x128_f8f6f4 v[44:47], v[0:7], v[214:221], v[44:47]
	v_mfma_f32_16x16x128_f8f6f4 v[40:43], v[8:15], v[214:221], v[40:43]
	s_setprio 0
	s_setprio 1
	v_mfma_f32_16x16x128_f8f6f4 v[84:87], v[16:23], v[190:197], v[84:87]
	v_mfma_f32_16x16x128_f8f6f4 v[80:83], v[24:31], v[190:197], v[80:83]
	v_mfma_f32_16x16x128_f8f6f4 v[68:71], v[16:23], v[198:205], v[68:71]
	v_mfma_f32_16x16x128_f8f6f4 v[64:67], v[24:31], v[198:205], v[64:67]
	v_mfma_f32_16x16x128_f8f6f4 v[52:55], v[16:23], v[206:213], v[52:55]
	v_mfma_f32_16x16x128_f8f6f4 v[48:51], v[24:31], v[206:213], v[48:51]
	v_mfma_f32_16x16x128_f8f6f4 v[36:39], v[16:23], v[214:221], v[36:39]
	v_mfma_f32_16x16x128_f8f6f4 v[32:35], v[24:31], v[214:221], v[32:35]
	s_setprio 0
	s_add_i32 s35, s35, 2
	s_add_u32 s44, s44, 0x100
	s_addc_u32 s45, s45, 0
	s_add_u32 s21, s21, 0x100
	s_addc_u32 s23, s23, 0
	s_cmp_gt_u32 s35, 13
	s_barrier
	s_cbranch_scc1 .LBB0_1273
